# P9 gate/up epilogue: 16 dwordx2 stores per wave widened to 8 dwordx4 via v_permlane16_swap between lane rows (same bytes, same addresses)
# baseline (speedup 1.0000x reference)
; DI float sigmoidf_(float x) { return __builtin_amdgcn_rcpf(1.0f + __expf(-x)); }
; DI unsigned cvt_pk_bf16(float lo, float hi) { unsigned r; asm volatile("v_cvt_pk_bf16_f32 %0, %1, %2" : "=v"(r) : "v"(lo), "v"(hi)); return r; }
;     DI void operator()(const f32x4 (&acc)[2][2][4][2], const pg8::Unit& u, int wr, int wc, int fr, int fq) const {
;         const int row0 = u.pm * 256 + wr * 64 + fr, pnr = u.pn & 3;
; #pragma unroll
;         for (int ai = 0; ai < 2; ++ai)
; #pragma unroll
;             for (int m = 0; m < 4; ++m) {
;                 const int p = row0 + ai * 128 + m * 16; const float r = rowr2[p];
; #pragma unroll
;                 for (int bj = 0; bj < 2; ++bj) {
;                     const int f0 = 128 * pnr + 64 * bj + 16 * wc + 4 * fq;
;                     float o[4];
; #pragma unroll
;                     for (int e = 0; e < 4; ++e) { const float g = acc[ai][bj][m][0][e] * r, up = acc[ai][bj][m][1][e] * r; o[e] = g * sigmoidf_(g) * up; }
;                     u32x2 w; w.x = pg8::cvt_pk_bf16(o[0], o[1]); w.y = pg8::cvt_pk_bf16(o[2], o[3]);
;                     *(u32x2*)(U + (size_t)p * FF + f0) = w;
;                 }
.LBB0_910:
	v_bfe_u32 v242, v0, 4, 1
	v_mul_u32_u24_e32 v242, 0x78, v242
	v_mov_b32_e32 v243, 0
	v_lshl_add_u32 v164, s63, 8, v154
	v_ashrrev_i32_e32 v165, 31, v164
	v_lshl_add_u64 v[166:167], v[164:165], 2, s[10:11]
	global_load_dword v176, v[166:167], off
	v_or_b32_e32 v168, 16, v164
	v_ashrrev_i32_e32 v169, 31, v168
	v_lshl_add_u64 v[170:171], v[168:169], 2, s[10:11]
	global_load_dword v178, v[170:171], off
	v_or_b32_e32 v168, 32, v164
	v_ashrrev_i32_e32 v169, 31, v168
	v_lshl_add_u64 v[170:171], v[168:169], 2, s[10:11]
	global_load_dword v180, v[170:171], off
	v_or_b32_e32 v168, 48, v164
	v_ashrrev_i32_e32 v169, 31, v168
	v_lshl_add_u64 v[164:165], v[168:169], 2, s[10:11]
	global_load_dword v182, v[164:165], off
	global_load_dword v184, v[166:167], off offset:512
	global_load_dword v186, v[166:167], off offset:576
	global_load_dword v188, v[166:167], off offset:640
	global_load_dword v190, v[166:167], off offset:704
	v_lshl_add_u32 v142, s63, 8, v154
	v_ashrrev_i32_e32 v143, 31, v142
	v_lshl_add_u64 v[140:141], v[142:143], 2, s[10:11]
	s_nop 0
	v_mov_b32_e32 v146, v126
	v_mov_b32_e32 v147, v122
	v_mov_b32_e32 v122, v127
	v_mov_b32_e32 v126, v128
	v_mov_b32_e32 v127, v124
	v_mov_b32_e32 v124, v129
	v_mov_b32_e32 v129, v114
	v_mov_b32_e32 v114, v119
	v_mov_b32_e32 v128, v118
	v_mov_b32_e32 v148, v120
	v_mov_b32_e32 v149, v116
	v_mov_b32_e32 v116, v121
	v_lshlrev_b64 v[118:119], 10, v[142:143]
	s_lshl_b32 s29, s34, 7
	s_and_b32 s29, s29, 0x180
	v_or_b32_e32 v134, s29, v156
	v_or_b32_e32 v120, 16, v142
	v_lshl_add_u64 v[118:119], s[12:13], 0, v[118:119]
	v_lshlrev_b32_e32 v134, 1, v134
	v_ashrrev_i32_e32 v121, 31, v120
	v_lshl_add_u64 v[118:119], v[118:119], 0, v[134:135]
	v_lshl_add_u64 v[150:151], v[120:121], 2, s[10:11]
	v_lshlrev_b64 v[120:121], 10, v[120:121]
	v_lshl_add_u64 v[120:121], s[12:13], 0, v[120:121]
	v_lshl_add_u64 v[120:121], v[120:121], 0, v[134:135]
	s_nop 0
	s_waitcnt vmcnt(7)
	v_pk_mul_f32 v[146:147], v[146:147], v[176:177] op_sel_hi:[1,0]
	v_pk_mul_f32 v[122:123], v[122:123], v[176:177] op_sel_hi:[1,0]
	v_pk_mul_f32 v[126:127], v[126:127], v[176:177] op_sel_hi:[1,0]
	v_pk_mul_f32 v[124:125], v[124:125], v[176:177] op_sel_hi:[1,0]
	v_pk_mul_f32 v[114:115], v[114:115], v[176:177] op_sel_hi:[1,0]
	v_pk_mul_f32 v[128:129], v[128:129], v[176:177] op_sel_hi:[1,0]
	v_pk_mul_f32 v[148:149], v[148:149], v[176:177] op_sel_hi:[1,0]
	v_pk_mul_f32 v[116:117], v[116:117], v[176:177] op_sel_hi:[1,0]
	v_mul_f32_e32 v137, 0xbfb8aa3b, v147
	v_mul_f32_e32 v139, 0xbfb8aa3b, v123
	v_mul_f32_e32 v143, 0xbfb8aa3b, v127
	v_mul_f32_e32 v144, 0xbfb8aa3b, v125
	v_mul_f32_e32 v160, 0xbfb8aa3b, v115
	v_mul_f32_e32 v145, 0xbfb8aa3b, v129
	v_mul_f32_e32 v161, 0xbfb8aa3b, v149
	v_mul_f32_e32 v162, 0xbfb8aa3b, v117
	v_exp_f32_e32 v137, v137
	v_exp_f32_e32 v139, v139
	v_exp_f32_e32 v143, v143
	v_exp_f32_e32 v144, v144
	v_exp_f32_e32 v160, v160
	v_exp_f32_e32 v145, v145
	v_exp_f32_e32 v161, v161
	v_exp_f32_e32 v162, v162
	v_add_f32_e32 v137, 1.0, v137
	v_add_f32_e32 v139, 1.0, v139
	v_add_f32_e32 v143, 1.0, v143
	v_add_f32_e32 v144, 1.0, v144
	v_add_f32_e32 v160, 1.0, v160
	v_add_f32_e32 v145, 1.0, v145
	v_add_f32_e32 v161, 1.0, v161
	v_add_f32_e32 v162, 1.0, v162
	v_rcp_f32_e32 v137, v137
	v_rcp_f32_e32 v139, v139
	v_rcp_f32_e32 v143, v143
	v_rcp_f32_e32 v144, v144
	v_rcp_f32_e32 v160, v160
	v_rcp_f32_e32 v145, v145
	v_rcp_f32_e32 v161, v161
	v_rcp_f32_e32 v162, v162
	v_mul_f32_e32 v137, v147, v137
	v_mul_f32_e32 v123, v123, v139
	v_mul_f32_e32 v127, v127, v143
	v_mul_f32_e32 v125, v125, v144
	v_mul_f32_e32 v115, v115, v160
	v_mul_f32_e32 v129, v129, v145
	v_mul_f32_e32 v139, v149, v161
	v_mul_f32_e32 v117, v117, v162
	v_mul_f32_e32 v137, v146, v137
	v_mul_f32_e32 v122, v122, v123
	v_mul_f32_e32 v123, v126, v127
	v_mul_f32_e32 v124, v124, v125
	v_mul_f32_e32 v126, v114, v115
	v_cvt_pk_bf16_f32 v232, v137, v122
	v_cvt_pk_bf16_f32 v233, v123, v124
	v_mul_f32_e32 v125, v128, v129
	v_mul_f32_e32 v127, v148, v139
	v_mul_f32_e32 v116, v116, v117
	v_cvt_pk_bf16_f32 v234, v125, v126
	v_cvt_pk_bf16_f32 v235, v127, v116
	s_nop 1
	v_permlane16_swap_b32_e32 v232, v234
	v_permlane16_swap_b32_e32 v233, v235
	v_lshl_add_u64 v[240:241], v[118:119], 0, v[242:243]
	global_store_dwordx4 v[240:241], v[232:235], off
	s_nop 0
	v_mov_b32_e32 v116, v110
	v_mov_b32_e32 v117, v106
	v_mov_b32_e32 v106, v111
	v_mov_b32_e32 v110, v112
	v_mov_b32_e32 v111, v108
	v_mov_b32_e32 v108, v113
	v_mov_b32_e32 v113, v98
	v_mov_b32_e32 v98, v103
	v_mov_b32_e32 v112, v102
	v_mov_b32_e32 v102, v104
	v_mov_b32_e32 v103, v100
	v_mov_b32_e32 v100, v105
	v_or_b32_e32 v104, 32, v142
	v_ashrrev_i32_e32 v105, 31, v104
	v_lshl_add_u64 v[122:123], v[104:105], 2, s[10:11]
	s_nop 0
	s_waitcnt vmcnt(7)
; DI float sigmoidf_(float x) { return __builtin_amdgcn_rcpf(1.0f + __expf(-x)); }
; DI unsigned cvt_pk_bf16(float lo, float hi) { unsigned r; asm volatile("v_cvt_pk_bf16_f32 %0, %1, %2" : "=v"(r) : "v"(lo), "v"(hi)); return r; }
;     DI void operator()(const f32x4 (&acc)[2][2][4][2], const pg8::Unit& u, int wr, int wc, int fr, int fq) const {
;     ...
;             for (int m = 0; m < 4; ++m) {
;                 const int p = row0 + ai * 128 + m * 16; const float r = rowr2[p];
; #pragma unroll
;                 for (int bj = 0; bj < 2; ++bj) {
;                     const int f0 = 128 * pnr + 64 * bj + 16 * wc + 4 * fq;
;                     float o[4];
; #pragma unroll
;                     for (int e = 0; e < 4; ++e) { const float g = acc[ai][bj][m][0][e] * r, up = acc[ai][bj][m][1][e] * r; o[e] = g * sigmoidf_(g) * up; }
;                     u32x2 w; w.x = pg8::cvt_pk_bf16(o[0], o[1]); w.y = pg8::cvt_pk_bf16(o[2], o[3]);
;                     *(u32x2*)(U + (size_t)p * FF + f0) = w;
;                 }
	v_pk_mul_f32 v[116:117], v[116:117], v[178:179] op_sel_hi:[1,0]
	v_pk_mul_f32 v[106:107], v[106:107], v[178:179] op_sel_hi:[1,0]
	v_pk_mul_f32 v[110:111], v[110:111], v[178:179] op_sel_hi:[1,0]
	v_pk_mul_f32 v[108:109], v[108:109], v[178:179] op_sel_hi:[1,0]
	v_pk_mul_f32 v[98:99], v[98:99], v[178:179] op_sel_hi:[1,0]
	v_pk_mul_f32 v[112:113], v[112:113], v[178:179] op_sel_hi:[1,0]
	v_pk_mul_f32 v[102:103], v[102:103], v[178:179] op_sel_hi:[1,0]
	v_pk_mul_f32 v[100:101], v[100:101], v[178:179] op_sel_hi:[1,0]
	v_mul_f32_e32 v114, 0xbfb8aa3b, v117
	v_mul_f32_e32 v115, 0xbfb8aa3b, v107
	v_mul_f32_e32 v124, 0xbfb8aa3b, v111
	v_mul_f32_e32 v125, 0xbfb8aa3b, v109
	v_mul_f32_e32 v127, 0xbfb8aa3b, v99
	v_mul_f32_e32 v126, 0xbfb8aa3b, v113
	v_mul_f32_e32 v128, 0xbfb8aa3b, v103
	v_mul_f32_e32 v129, 0xbfb8aa3b, v101
	v_exp_f32_e32 v114, v114
	v_exp_f32_e32 v115, v115
	v_exp_f32_e32 v124, v124
	v_exp_f32_e32 v125, v125
	v_exp_f32_e32 v127, v127
	v_exp_f32_e32 v126, v126
	v_exp_f32_e32 v128, v128
	v_exp_f32_e32 v129, v129
	v_add_f32_e32 v114, 1.0, v114
	v_add_f32_e32 v115, 1.0, v115
	v_add_f32_e32 v124, 1.0, v124
	v_add_f32_e32 v125, 1.0, v125
	v_add_f32_e32 v127, 1.0, v127
	v_add_f32_e32 v126, 1.0, v126
	v_add_f32_e32 v128, 1.0, v128
	v_add_f32_e32 v129, 1.0, v129
	v_rcp_f32_e32 v114, v114
	v_rcp_f32_e32 v115, v115
	v_rcp_f32_e32 v124, v124
	v_rcp_f32_e32 v125, v125
	v_rcp_f32_e32 v127, v127
	v_rcp_f32_e32 v126, v126
	v_rcp_f32_e32 v128, v128
	v_rcp_f32_e32 v129, v129
	v_mul_f32_e32 v114, v117, v114
	v_mul_f32_e32 v107, v107, v115
	v_mul_f32_e32 v111, v111, v124
	v_mul_f32_e32 v109, v109, v125
	v_mul_f32_e32 v99, v99, v127
	v_mul_f32_e32 v113, v113, v126
	v_mul_f32_e32 v103, v103, v128
	v_mul_f32_e32 v101, v101, v129
	v_mul_f32_e32 v114, v116, v114
	v_mul_f32_e32 v106, v106, v107
	v_mul_f32_e32 v107, v110, v111
	v_mul_f32_e32 v108, v108, v109
	v_mul_f32_e32 v110, v98, v99
	v_cvt_pk_bf16_f32 v236, v114, v106
	v_cvt_pk_bf16_f32 v237, v107, v108
	v_mul_f32_e32 v109, v112, v113
	v_mul_f32_e32 v102, v102, v103
	v_mul_f32_e32 v100, v100, v101
	v_cvt_pk_bf16_f32 v238, v109, v110
	v_cvt_pk_bf16_f32 v239, v102, v100
	s_nop 1
	v_permlane16_swap_b32_e32 v236, v238
	v_permlane16_swap_b32_e32 v237, v239
	v_lshl_add_u64 v[240:241], v[120:121], 0, v[242:243]
	global_store_dwordx4 v[240:241], v[236:239], off
	s_nop 0
	v_mov_b32_e32 v100, v94
	v_mov_b32_e32 v101, v90
	v_mov_b32_e32 v90, v95
	v_mov_b32_e32 v94, v96
	v_mov_b32_e32 v95, v92
	v_mov_b32_e32 v92, v97
	v_mov_b32_e32 v97, v82
	v_mov_b32_e32 v82, v87
	v_mov_b32_e32 v96, v86
	v_mov_b32_e32 v86, v88
	v_mov_b32_e32 v87, v84
	v_mov_b32_e32 v84, v89
	v_lshlrev_b64 v[102:103], 10, v[104:105]
	v_or_b32_e32 v88, 48, v142
	v_lshl_add_u64 v[102:103], s[12:13], 0, v[102:103]
	v_ashrrev_i32_e32 v89, 31, v88
	v_lshl_add_u64 v[102:103], v[102:103], 0, v[134:135]
	v_lshl_add_u64 v[104:105], v[88:89], 2, s[10:11]
	s_nop 0
	s_waitcnt vmcnt(7)
	v_pk_mul_f32 v[100:101], v[100:101], v[180:181] op_sel_hi:[1,0]
	v_pk_mul_f32 v[90:91], v[90:91], v[180:181] op_sel_hi:[1,0]
	v_pk_mul_f32 v[94:95], v[94:95], v[180:181] op_sel_hi:[1,0]
	v_pk_mul_f32 v[92:93], v[92:93], v[180:181] op_sel_hi:[1,0]
	v_pk_mul_f32 v[82:83], v[82:83], v[180:181] op_sel_hi:[1,0]
	v_pk_mul_f32 v[96:97], v[96:97], v[180:181] op_sel_hi:[1,0]
	v_pk_mul_f32 v[86:87], v[86:87], v[180:181] op_sel_hi:[1,0]
	v_pk_mul_f32 v[84:85], v[84:85], v[180:181] op_sel_hi:[1,0]
	v_mul_f32_e32 v98, 0xbfb8aa3b, v101
	v_mul_f32_e32 v99, 0xbfb8aa3b, v91
	v_mul_f32_e32 v106, 0xbfb8aa3b, v95
	v_mul_f32_e32 v107, 0xbfb8aa3b, v93
	v_mul_f32_e32 v109, 0xbfb8aa3b, v83
	v_mul_f32_e32 v108, 0xbfb8aa3b, v97
	v_mul_f32_e32 v110, 0xbfb8aa3b, v87
	v_mul_f32_e32 v111, 0xbfb8aa3b, v85
	v_exp_f32_e32 v98, v98
	v_exp_f32_e32 v99, v99
	v_exp_f32_e32 v106, v106
	v_exp_f32_e32 v107, v107
	v_exp_f32_e32 v109, v109
	v_exp_f32_e32 v108, v108
	v_exp_f32_e32 v110, v110
	v_exp_f32_e32 v111, v111
	v_add_f32_e32 v98, 1.0, v98
	v_add_f32_e32 v99, 1.0, v99
	v_add_f32_e32 v106, 1.0, v106
	v_add_f32_e32 v107, 1.0, v107
	v_add_f32_e32 v109, 1.0, v109
	v_add_f32_e32 v108, 1.0, v108
	v_add_f32_e32 v110, 1.0, v110
	v_add_f32_e32 v111, 1.0, v111
	v_rcp_f32_e32 v98, v98
	v_rcp_f32_e32 v99, v99
	v_rcp_f32_e32 v106, v106
	v_rcp_f32_e32 v107, v107
	v_rcp_f32_e32 v109, v109
	v_rcp_f32_e32 v108, v108
	v_rcp_f32_e32 v110, v110
	v_rcp_f32_e32 v111, v111
	v_mul_f32_e32 v98, v101, v98
	v_mul_f32_e32 v91, v91, v99
	v_mul_f32_e32 v95, v95, v106
	v_mul_f32_e32 v93, v93, v107
	v_mul_f32_e32 v83, v83, v109
	v_mul_f32_e32 v97, v97, v108
	v_mul_f32_e32 v87, v87, v110
	v_mul_f32_e32 v85, v85, v111
	v_mul_f32_e32 v98, v100, v98
	v_mul_f32_e32 v90, v90, v91
	v_mul_f32_e32 v91, v94, v95
	v_mul_f32_e32 v92, v92, v93
	v_mul_f32_e32 v94, v82, v83
	v_cvt_pk_bf16_f32 v232, v98, v90
	v_cvt_pk_bf16_f32 v233, v91, v92
	v_mul_f32_e32 v93, v96, v97
	v_mul_f32_e32 v86, v86, v87
	v_mul_f32_e32 v84, v84, v85
	v_cvt_pk_bf16_f32 v234, v93, v94
	v_cvt_pk_bf16_f32 v235, v86, v84
	s_nop 1
	v_permlane16_swap_b32_e32 v232, v234
	v_permlane16_swap_b32_e32 v233, v235
	v_lshl_add_u64 v[240:241], v[102:103], 0, v[242:243]
	global_store_dwordx4 v[240:241], v[232:235], off
	s_nop 0
	v_mov_b32_e32 v84, v78
	v_mov_b32_e32 v85, v74
	v_mov_b32_e32 v74, v79
	v_mov_b32_e32 v78, v80
	v_mov_b32_e32 v79, v76
	v_mov_b32_e32 v76, v81
	v_mov_b32_e32 v81, v66
	v_mov_b32_e32 v66, v71
	v_mov_b32_e32 v80, v70
	v_mov_b32_e32 v70, v72
	v_mov_b32_e32 v71, v68
	v_mov_b32_e32 v68, v73
	v_lshlrev_b64 v[72:73], 10, v[88:89]
	v_lshl_add_u64 v[72:73], s[12:13], 0, v[72:73]
	v_lshl_add_u64 v[72:73], v[72:73], 0, v[134:135]
	s_nop 0
	s_waitcnt vmcnt(7)
; DI float sigmoidf_(float x) { return __builtin_amdgcn_rcpf(1.0f + __expf(-x)); }
; DI unsigned cvt_pk_bf16(float lo, float hi) { unsigned r; asm volatile("v_cvt_pk_bf16_f32 %0, %1, %2" : "=v"(r) : "v"(lo), "v"(hi)); return r; }
;     DI void operator()(const f32x4 (&acc)[2][2][4][2], const pg8::Unit& u, int wr, int wc, int fr, int fq) const {
;     ...
;             for (int m = 0; m < 4; ++m) {
;                 const int p = row0 + ai * 128 + m * 16; const float r = rowr2[p];
; #pragma unroll
;                 for (int bj = 0; bj < 2; ++bj) {
;                     const int f0 = 128 * pnr + 64 * bj + 16 * wc + 4 * fq;
;                     float o[4];
; #pragma unroll
;                     for (int e = 0; e < 4; ++e) { const float g = acc[ai][bj][m][0][e] * r, up = acc[ai][bj][m][1][e] * r; o[e] = g * sigmoidf_(g) * up; }
;                     u32x2 w; w.x = pg8::cvt_pk_bf16(o[0], o[1]); w.y = pg8::cvt_pk_bf16(o[2], o[3]);
;                     *(u32x2*)(U + (size_t)p * FF + f0) = w;
;                 }
	v_pk_mul_f32 v[84:85], v[84:85], v[182:183] op_sel_hi:[1,0]
	v_pk_mul_f32 v[74:75], v[74:75], v[182:183] op_sel_hi:[1,0]
	v_pk_mul_f32 v[78:79], v[78:79], v[182:183] op_sel_hi:[1,0]
	v_pk_mul_f32 v[76:77], v[76:77], v[182:183] op_sel_hi:[1,0]
	v_pk_mul_f32 v[66:67], v[66:67], v[182:183] op_sel_hi:[1,0]
	v_pk_mul_f32 v[80:81], v[80:81], v[182:183] op_sel_hi:[1,0]
	v_pk_mul_f32 v[70:71], v[70:71], v[182:183] op_sel_hi:[1,0]
	v_pk_mul_f32 v[68:69], v[68:69], v[182:183] op_sel_hi:[1,0]
	v_mul_f32_e32 v82, 0xbfb8aa3b, v85
	v_mul_f32_e32 v83, 0xbfb8aa3b, v75
	v_mul_f32_e32 v86, 0xbfb8aa3b, v79
	v_mul_f32_e32 v87, 0xbfb8aa3b, v77
	v_mul_f32_e32 v89, 0xbfb8aa3b, v67
	v_mul_f32_e32 v88, 0xbfb8aa3b, v81
	v_mul_f32_e32 v90, 0xbfb8aa3b, v71
	v_mul_f32_e32 v91, 0xbfb8aa3b, v69
	v_exp_f32_e32 v82, v82
	v_exp_f32_e32 v83, v83
	v_exp_f32_e32 v86, v86
	v_exp_f32_e32 v87, v87
	v_exp_f32_e32 v89, v89
	v_exp_f32_e32 v88, v88
	v_exp_f32_e32 v90, v90
	v_exp_f32_e32 v91, v91
	v_add_f32_e32 v82, 1.0, v82
	v_add_f32_e32 v83, 1.0, v83
	v_add_f32_e32 v86, 1.0, v86
	v_add_f32_e32 v87, 1.0, v87
	v_add_f32_e32 v89, 1.0, v89
	v_add_f32_e32 v88, 1.0, v88
	v_add_f32_e32 v90, 1.0, v90
	v_add_f32_e32 v91, 1.0, v91
	v_rcp_f32_e32 v82, v82
	v_rcp_f32_e32 v83, v83
	v_rcp_f32_e32 v86, v86
	v_rcp_f32_e32 v87, v87
	v_rcp_f32_e32 v89, v89
	v_rcp_f32_e32 v88, v88
	v_rcp_f32_e32 v90, v90
	v_rcp_f32_e32 v91, v91
	v_mul_f32_e32 v82, v85, v82
	v_mul_f32_e32 v75, v75, v83
	v_mul_f32_e32 v79, v79, v86
	v_mul_f32_e32 v77, v77, v87
	v_mul_f32_e32 v67, v67, v89
	v_mul_f32_e32 v81, v81, v88
	v_mul_f32_e32 v71, v71, v90
	v_mul_f32_e32 v69, v69, v91
	v_mul_f32_e32 v82, v84, v82
	v_mul_f32_e32 v74, v74, v75
	v_mul_f32_e32 v75, v78, v79
	v_mul_f32_e32 v76, v76, v77
	v_mul_f32_e32 v78, v66, v67
	v_cvt_pk_bf16_f32 v236, v82, v74
	v_cvt_pk_bf16_f32 v237, v75, v76
	v_mul_f32_e32 v77, v80, v81
	v_mul_f32_e32 v70, v70, v71
	v_mul_f32_e32 v68, v68, v69
	v_cvt_pk_bf16_f32 v238, v77, v78
	v_cvt_pk_bf16_f32 v239, v70, v68
	s_nop 1
	v_permlane16_swap_b32_e32 v236, v238
	v_permlane16_swap_b32_e32 v237, v239
	v_lshl_add_u64 v[240:241], v[72:73], 0, v[242:243]
	global_store_dwordx4 v[240:241], v[236:239], off
	s_nop 0
	v_mov_b32_e32 v68, v62
	v_mov_b32_e32 v69, v58
	v_mov_b32_e32 v58, v63
	v_mov_b32_e32 v62, v64
	v_mov_b32_e32 v63, v60
	v_mov_b32_e32 v60, v65
	v_mov_b32_e32 v65, v50
	v_mov_b32_e32 v50, v55
	v_mov_b32_e32 v64, v54
	v_mov_b32_e32 v54, v56
	v_mov_b32_e32 v55, v52
	v_mov_b32_e32 v52, v57
	v_add_co_u32_e32 v70, vcc, s49, v118
	v_lshl_add_u64 v[56:57], v[118:119], 0, s[20:21]
	s_nop 0
	v_addc_co_u32_e32 v71, vcc, 0, v119, vcc
	s_nop 0
	s_waitcnt vmcnt(7)
	v_pk_mul_f32 v[68:69], v[68:69], v[184:185] op_sel_hi:[1,0]
	v_pk_mul_f32 v[58:59], v[58:59], v[184:185] op_sel_hi:[1,0]
	v_pk_mul_f32 v[62:63], v[62:63], v[184:185] op_sel_hi:[1,0]
	v_pk_mul_f32 v[60:61], v[60:61], v[184:185] op_sel_hi:[1,0]
	v_pk_mul_f32 v[50:51], v[50:51], v[184:185] op_sel_hi:[1,0]
	v_pk_mul_f32 v[64:65], v[64:65], v[184:185] op_sel_hi:[1,0]
	v_pk_mul_f32 v[54:55], v[54:55], v[184:185] op_sel_hi:[1,0]
	v_pk_mul_f32 v[52:53], v[52:53], v[184:185] op_sel_hi:[1,0]
	v_mul_f32_e32 v66, 0xbfb8aa3b, v69
	v_mul_f32_e32 v67, 0xbfb8aa3b, v59
	v_mul_f32_e32 v72, 0xbfb8aa3b, v63
	v_mul_f32_e32 v73, 0xbfb8aa3b, v61
	v_mul_f32_e32 v75, 0xbfb8aa3b, v51
	v_mul_f32_e32 v74, 0xbfb8aa3b, v65
	v_mul_f32_e32 v76, 0xbfb8aa3b, v55
	v_mul_f32_e32 v77, 0xbfb8aa3b, v53
	v_exp_f32_e32 v66, v66
	v_exp_f32_e32 v67, v67
	v_exp_f32_e32 v72, v72
	v_exp_f32_e32 v73, v73
	v_exp_f32_e32 v75, v75
	v_exp_f32_e32 v74, v74
	v_exp_f32_e32 v76, v76
	v_exp_f32_e32 v77, v77
	v_add_f32_e32 v66, 1.0, v66
	v_add_f32_e32 v67, 1.0, v67
	v_add_f32_e32 v72, 1.0, v72
	v_add_f32_e32 v73, 1.0, v73
	v_add_f32_e32 v75, 1.0, v75
	v_add_f32_e32 v74, 1.0, v74
	v_add_f32_e32 v76, 1.0, v76
	v_add_f32_e32 v77, 1.0, v77
	v_rcp_f32_e32 v66, v66
	v_rcp_f32_e32 v67, v67
	v_rcp_f32_e32 v72, v72
	v_rcp_f32_e32 v73, v73
	v_rcp_f32_e32 v75, v75
	v_rcp_f32_e32 v74, v74
	v_rcp_f32_e32 v76, v76
	v_rcp_f32_e32 v77, v77
	v_mul_f32_e32 v66, v69, v66
	v_mul_f32_e32 v59, v59, v67
	v_mul_f32_e32 v63, v63, v72
	v_mul_f32_e32 v61, v61, v73
	v_mul_f32_e32 v51, v51, v75
	v_mul_f32_e32 v65, v65, v74
	v_mul_f32_e32 v55, v55, v76
	v_mul_f32_e32 v53, v53, v77
	v_mul_f32_e32 v66, v68, v66
	v_mul_f32_e32 v58, v58, v59
	v_mul_f32_e32 v59, v62, v63
	v_mul_f32_e32 v60, v60, v61
	v_mul_f32_e32 v62, v50, v51
	v_cvt_pk_bf16_f32 v232, v66, v58
	v_cvt_pk_bf16_f32 v233, v59, v60
	v_mul_f32_e32 v61, v64, v65
	v_mul_f32_e32 v54, v54, v55
	v_mul_f32_e32 v52, v52, v53
	v_cvt_pk_bf16_f32 v234, v61, v62
	v_cvt_pk_bf16_f32 v235, v54, v52
	s_nop 1
	v_permlane16_swap_b32_e32 v232, v234
	v_permlane16_swap_b32_e32 v233, v235
	v_lshl_add_u64 v[240:241], v[56:57], 0, v[242:243]
	global_store_dwordx4 v[240:241], v[232:235], off
	s_nop 0
	v_mov_b32_e32 v52, v46
	v_mov_b32_e32 v53, v42
	v_mov_b32_e32 v42, v47
	v_mov_b32_e32 v46, v48
	v_mov_b32_e32 v47, v44
	v_mov_b32_e32 v44, v49
	v_mov_b32_e32 v49, v34
	v_mov_b32_e32 v34, v39
	v_mov_b32_e32 v48, v38
	v_mov_b32_e32 v38, v40
	v_mov_b32_e32 v39, v36
	v_mov_b32_e32 v36, v41
	v_add_co_u32_e32 v54, vcc, s55, v118
	v_lshl_add_u64 v[40:41], v[118:119], 0, s[22:23]
	s_nop 0
	v_addc_co_u32_e32 v55, vcc, 0, v119, vcc
	s_nop 0
	s_waitcnt vmcnt(7)
; DI float sigmoidf_(float x) { return __builtin_amdgcn_rcpf(1.0f + __expf(-x)); }
; DI unsigned cvt_pk_bf16(float lo, float hi) { unsigned r; asm volatile("v_cvt_pk_bf16_f32 %0, %1, %2" : "=v"(r) : "v"(lo), "v"(hi)); return r; }
;     DI void operator()(const f32x4 (&acc)[2][2][4][2], const pg8::Unit& u, int wr, int wc, int fr, int fq) const {
;     ...
;             for (int m = 0; m < 4; ++m) {
;                 const int p = row0 + ai * 128 + m * 16; const float r = rowr2[p];
; #pragma unroll
;                 for (int bj = 0; bj < 2; ++bj) {
;                     const int f0 = 128 * pnr + 64 * bj + 16 * wc + 4 * fq;
;                     float o[4];
; #pragma unroll
;                     for (int e = 0; e < 4; ++e) { const float g = acc[ai][bj][m][0][e] * r, up = acc[ai][bj][m][1][e] * r; o[e] = g * sigmoidf_(g) * up; }
;                     u32x2 w; w.x = pg8::cvt_pk_bf16(o[0], o[1]); w.y = pg8::cvt_pk_bf16(o[2], o[3]);
;                     *(u32x2*)(U + (size_t)p * FF + f0) = w;
;                 }
	v_pk_mul_f32 v[52:53], v[52:53], v[186:187] op_sel_hi:[1,0]
	v_pk_mul_f32 v[42:43], v[42:43], v[186:187] op_sel_hi:[1,0]
	v_pk_mul_f32 v[46:47], v[46:47], v[186:187] op_sel_hi:[1,0]
	v_pk_mul_f32 v[44:45], v[44:45], v[186:187] op_sel_hi:[1,0]
	v_pk_mul_f32 v[34:35], v[34:35], v[186:187] op_sel_hi:[1,0]
	v_pk_mul_f32 v[48:49], v[48:49], v[186:187] op_sel_hi:[1,0]
	v_pk_mul_f32 v[38:39], v[38:39], v[186:187] op_sel_hi:[1,0]
	v_pk_mul_f32 v[36:37], v[36:37], v[186:187] op_sel_hi:[1,0]
	v_mul_f32_e32 v50, 0xbfb8aa3b, v53
	v_mul_f32_e32 v51, 0xbfb8aa3b, v43
	v_mul_f32_e32 v56, 0xbfb8aa3b, v47
	v_mul_f32_e32 v57, 0xbfb8aa3b, v45
	v_mul_f32_e32 v59, 0xbfb8aa3b, v35
	v_mul_f32_e32 v58, 0xbfb8aa3b, v49
	v_mul_f32_e32 v60, 0xbfb8aa3b, v39
	v_mul_f32_e32 v61, 0xbfb8aa3b, v37
	v_exp_f32_e32 v50, v50
	v_exp_f32_e32 v51, v51
	v_exp_f32_e32 v56, v56
	v_exp_f32_e32 v57, v57
	v_exp_f32_e32 v59, v59
	v_exp_f32_e32 v58, v58
	v_exp_f32_e32 v60, v60
	v_exp_f32_e32 v61, v61
	v_add_f32_e32 v50, 1.0, v50
	v_add_f32_e32 v51, 1.0, v51
	v_add_f32_e32 v56, 1.0, v56
	v_add_f32_e32 v57, 1.0, v57
	v_add_f32_e32 v59, 1.0, v59
	v_add_f32_e32 v58, 1.0, v58
	v_add_f32_e32 v60, 1.0, v60
	v_add_f32_e32 v61, 1.0, v61
	v_rcp_f32_e32 v50, v50
	v_rcp_f32_e32 v51, v51
	v_rcp_f32_e32 v56, v56
	v_rcp_f32_e32 v57, v57
	v_rcp_f32_e32 v59, v59
	v_rcp_f32_e32 v58, v58
	v_rcp_f32_e32 v60, v60
	v_rcp_f32_e32 v61, v61
	v_mul_f32_e32 v50, v53, v50
	v_mul_f32_e32 v43, v43, v51
	v_mul_f32_e32 v47, v47, v56
	v_mul_f32_e32 v45, v45, v57
	v_mul_f32_e32 v35, v35, v59
	v_mul_f32_e32 v49, v49, v58
	v_mul_f32_e32 v39, v39, v60
	v_mul_f32_e32 v37, v37, v61
	v_mul_f32_e32 v50, v52, v50
	v_mul_f32_e32 v42, v42, v43
	v_mul_f32_e32 v43, v46, v47
	v_mul_f32_e32 v44, v44, v45
	v_mul_f32_e32 v46, v34, v35
	v_cvt_pk_bf16_f32 v236, v50, v42
	v_cvt_pk_bf16_f32 v237, v43, v44
	v_mul_f32_e32 v45, v48, v49
	v_mul_f32_e32 v38, v38, v39
	v_mul_f32_e32 v36, v36, v37
	v_cvt_pk_bf16_f32 v238, v45, v46
	v_cvt_pk_bf16_f32 v239, v38, v36
	s_nop 1
	v_permlane16_swap_b32_e32 v236, v238
	v_permlane16_swap_b32_e32 v237, v239
	v_lshl_add_u64 v[240:241], v[40:41], 0, v[242:243]
	global_store_dwordx4 v[240:241], v[236:239], off
	s_nop 0
	v_mov_b32_e32 v36, v30
	v_mov_b32_e32 v37, v26
	v_mov_b32_e32 v26, v31
	v_mov_b32_e32 v30, v32
	v_mov_b32_e32 v31, v28
	v_mov_b32_e32 v28, v33
	v_mov_b32_e32 v33, v18
	v_mov_b32_e32 v18, v23
	v_mov_b32_e32 v32, v22
	v_mov_b32_e32 v22, v24
	v_mov_b32_e32 v23, v20
	v_mov_b32_e32 v20, v25
	v_add_co_u32_e32 v38, vcc, s56, v118
	v_lshl_add_u64 v[24:25], v[118:119], 0, s[24:25]
	s_nop 0
	v_addc_co_u32_e32 v39, vcc, 0, v119, vcc
	s_and_b64 vcc, exec, s[2:3]
	s_nop 0
	s_waitcnt vmcnt(7)
; DI float sigmoidf_(float x) { return __builtin_amdgcn_rcpf(1.0f + __expf(-x)); }
; DI unsigned cvt_pk_bf16(float lo, float hi) { unsigned r; asm volatile("v_cvt_pk_bf16_f32 %0, %1, %2" : "=v"(r) : "v"(lo), "v"(hi)); return r; }
; #define PG8_BAR __builtin_amdgcn_s_barrier()
; template <class Epi, class Sched, bool ALIGN_EPI, bool SP2, bool GATHER>
; DI void gemm_phase(LAS unsigned char* lds, const Gemm g, const Sched& S, const Epi& E) {
;     ...
;         if (!has_next) break;
; #pragma unroll
;         for (int a = 0; a < 2; ++a)
; #pragma unroll
;             for (int b = 0; b < 2; ++b)
; #pragma unroll
;                 for (int m = 0; m < 4; ++m)
; #pragma unroll
;                     for (int n = 0; n < 2; ++n) acc[a][b][m][n] = (f32x4){0.f, 0.f, 0.f, 0.f};
;         cur = nxt; cA = nA; cB = nB; ++ui;
; #pragma unroll
;         for (int h = 0; h < 2; ++h) { gC[h][0] = gN[h][0]; gC[h][1] = gN[h][1]; }
;         if constexpr (ALIGN_EPI) { if (wr == 1) PG8_BAR; }
;     DI void operator()(const f32x4 (&acc)[2][2][4][2], const pg8::Unit& u, int wr, int wc, int fr, int fq) const {
;     ...
;             for (int m = 0; m < 4; ++m) {
;                 const int p = row0 + ai * 128 + m * 16; const float r = rowr2[p];
; #pragma unroll
;                 for (int bj = 0; bj < 2; ++bj) {
;                     const int f0 = 128 * pnr + 64 * bj + 16 * wc + 4 * fq;
;                     float o[4];
; #pragma unroll
;                     for (int e = 0; e < 4; ++e) { const float g = acc[ai][bj][m][0][e] * r, up = acc[ai][bj][m][1][e] * r; o[e] = g * sigmoidf_(g) * up; }
;                     u32x2 w; w.x = pg8::cvt_pk_bf16(o[0], o[1]); w.y = pg8::cvt_pk_bf16(o[2], o[3]);
;                     *(u32x2*)(U + (size_t)p * FF + f0) = w;
;                 }
;             }
	v_pk_mul_f32 v[36:37], v[36:37], v[188:189] op_sel_hi:[1,0]
	v_pk_mul_f32 v[26:27], v[26:27], v[188:189] op_sel_hi:[1,0]
	v_pk_mul_f32 v[30:31], v[30:31], v[188:189] op_sel_hi:[1,0]
	v_pk_mul_f32 v[28:29], v[28:29], v[188:189] op_sel_hi:[1,0]
	v_pk_mul_f32 v[18:19], v[18:19], v[188:189] op_sel_hi:[1,0]
	v_pk_mul_f32 v[32:33], v[32:33], v[188:189] op_sel_hi:[1,0]
	v_pk_mul_f32 v[22:23], v[22:23], v[188:189] op_sel_hi:[1,0]
	v_pk_mul_f32 v[20:21], v[20:21], v[188:189] op_sel_hi:[1,0]
	v_mul_f32_e32 v34, 0xbfb8aa3b, v37
	v_mul_f32_e32 v35, 0xbfb8aa3b, v27
	v_mul_f32_e32 v40, 0xbfb8aa3b, v31
	v_mul_f32_e32 v41, 0xbfb8aa3b, v29
	v_mul_f32_e32 v43, 0xbfb8aa3b, v19
	v_mul_f32_e32 v42, 0xbfb8aa3b, v33
	v_mul_f32_e32 v44, 0xbfb8aa3b, v23
	v_mul_f32_e32 v45, 0xbfb8aa3b, v21
	v_exp_f32_e32 v34, v34
	v_exp_f32_e32 v35, v35
	v_exp_f32_e32 v40, v40
	v_exp_f32_e32 v41, v41
	v_exp_f32_e32 v43, v43
	v_exp_f32_e32 v42, v42
	v_exp_f32_e32 v44, v44
	v_exp_f32_e32 v45, v45
	v_add_f32_e32 v34, 1.0, v34
	v_add_f32_e32 v35, 1.0, v35
	v_add_f32_e32 v40, 1.0, v40
	v_add_f32_e32 v41, 1.0, v41
	v_add_f32_e32 v43, 1.0, v43
	v_add_f32_e32 v42, 1.0, v42
	v_add_f32_e32 v44, 1.0, v44
	v_add_f32_e32 v45, 1.0, v45
	v_rcp_f32_e32 v34, v34
	v_rcp_f32_e32 v35, v35
	v_rcp_f32_e32 v40, v40
	v_rcp_f32_e32 v41, v41
	v_rcp_f32_e32 v43, v43
	v_rcp_f32_e32 v42, v42
	v_rcp_f32_e32 v44, v44
	v_rcp_f32_e32 v45, v45
	v_mul_f32_e32 v34, v37, v34
	v_mul_f32_e32 v27, v27, v35
	v_mul_f32_e32 v31, v31, v40
	v_mul_f32_e32 v29, v29, v41
	v_mul_f32_e32 v19, v19, v43
	v_mul_f32_e32 v33, v33, v42
	v_mul_f32_e32 v23, v23, v44
	v_mul_f32_e32 v21, v21, v45
	v_mul_f32_e32 v34, v36, v34
	v_mul_f32_e32 v26, v26, v27
	v_mul_f32_e32 v27, v30, v31
	v_mul_f32_e32 v28, v28, v29
	v_mul_f32_e32 v30, v18, v19
	v_cvt_pk_bf16_f32 v232, v34, v26
	v_cvt_pk_bf16_f32 v233, v27, v28
	v_mul_f32_e32 v29, v32, v33
	v_mul_f32_e32 v22, v22, v23
	v_mul_f32_e32 v20, v20, v21
	v_cvt_pk_bf16_f32 v234, v29, v30
	v_cvt_pk_bf16_f32 v235, v22, v20
	s_nop 1
	v_permlane16_swap_b32_e32 v232, v234
	v_permlane16_swap_b32_e32 v233, v235
	v_lshl_add_u64 v[240:241], v[24:25], 0, v[242:243]
	global_store_dwordx4 v[240:241], v[232:235], off
	s_nop 0
	v_mov_b32_e32 v20, v14
	v_mov_b32_e32 v21, v10
	v_mov_b32_e32 v10, v15
	v_mov_b32_e32 v14, v16
	v_mov_b32_e32 v15, v12
	v_mov_b32_e32 v12, v17
	v_mov_b32_e32 v17, v2
	v_mov_b32_e32 v2, v7
	v_mov_b32_e32 v16, v6
	v_mov_b32_e32 v6, v8
	v_mov_b32_e32 v7, v4
	v_mov_b32_e32 v4, v9
	v_add_co_u32_e64 v22, s[2:3], s57, v118
	v_lshl_add_u64 v[8:9], v[118:119], 0, s[26:27]
	s_nop 0
	v_addc_co_u32_e64 v23, s[2:3], 0, v119, s[2:3]
	s_mov_b64 s[2:3], -1
	s_nop 0
	s_waitcnt vmcnt(7)
	v_pk_mul_f32 v[20:21], v[20:21], v[190:191] op_sel_hi:[1,0]
	v_pk_mul_f32 v[10:11], v[10:11], v[190:191] op_sel_hi:[1,0]
	v_pk_mul_f32 v[14:15], v[14:15], v[190:191] op_sel_hi:[1,0]
	v_pk_mul_f32 v[12:13], v[12:13], v[190:191] op_sel_hi:[1,0]
	v_pk_mul_f32 v[2:3], v[2:3], v[190:191] op_sel_hi:[1,0]
	v_pk_mul_f32 v[16:17], v[16:17], v[190:191] op_sel_hi:[1,0]
	v_pk_mul_f32 v[6:7], v[6:7], v[190:191] op_sel_hi:[1,0]
	v_pk_mul_f32 v[4:5], v[4:5], v[190:191] op_sel_hi:[1,0]
	v_mul_f32_e32 v18, 0xbfb8aa3b, v21
	v_mul_f32_e32 v19, 0xbfb8aa3b, v11
	v_mul_f32_e32 v24, 0xbfb8aa3b, v15
	v_mul_f32_e32 v25, 0xbfb8aa3b, v13
	v_mul_f32_e32 v27, 0xbfb8aa3b, v3
	v_mul_f32_e32 v26, 0xbfb8aa3b, v17
	v_mul_f32_e32 v28, 0xbfb8aa3b, v7
	v_mul_f32_e32 v29, 0xbfb8aa3b, v5
	v_exp_f32_e32 v18, v18
	v_exp_f32_e32 v19, v19
	v_exp_f32_e32 v24, v24
	v_exp_f32_e32 v25, v25
	v_exp_f32_e32 v27, v27
	v_exp_f32_e32 v26, v26
	v_exp_f32_e32 v28, v28
	v_exp_f32_e32 v29, v29
	v_add_f32_e32 v18, 1.0, v18
	v_add_f32_e32 v19, 1.0, v19
	v_add_f32_e32 v24, 1.0, v24
	v_add_f32_e32 v25, 1.0, v25
	v_add_f32_e32 v27, 1.0, v27
	v_add_f32_e32 v26, 1.0, v26
	v_add_f32_e32 v28, 1.0, v28
	v_add_f32_e32 v29, 1.0, v29
	v_rcp_f32_e32 v18, v18
	v_rcp_f32_e32 v19, v19
	v_rcp_f32_e32 v24, v24
	v_rcp_f32_e32 v25, v25
	v_rcp_f32_e32 v27, v27
	v_rcp_f32_e32 v26, v26
	v_rcp_f32_e32 v28, v28
	v_rcp_f32_e32 v29, v29
	v_mul_f32_e32 v18, v21, v18
	v_mul_f32_e32 v11, v11, v19
	v_mul_f32_e32 v15, v15, v24
	v_mul_f32_e32 v13, v13, v25
	v_mul_f32_e32 v3, v3, v27
	v_mul_f32_e32 v17, v17, v26
	v_mul_f32_e32 v7, v7, v28
	v_mul_f32_e32 v5, v5, v29
	v_mul_f32_e32 v18, v20, v18
	v_mul_f32_e32 v10, v10, v11
	v_mul_f32_e32 v11, v14, v15
	v_mul_f32_e32 v12, v12, v13
	v_mul_f32_e32 v14, v2, v3
	v_cvt_pk_bf16_f32 v236, v18, v10
	v_cvt_pk_bf16_f32 v237, v11, v12
	v_mul_f32_e32 v13, v16, v17
	v_mul_f32_e32 v6, v6, v7
	v_mul_f32_e32 v4, v4, v5
	v_cvt_pk_bf16_f32 v238, v13, v14
	v_cvt_pk_bf16_f32 v239, v6, v4
	s_nop 1
	v_permlane16_swap_b32_e32 v236, v238
	v_permlane16_swap_b32_e32 v237, v239
	v_lshl_add_u64 v[240:241], v[8:9], 0, v[242:243]
	global_store_dwordx4 v[240:241], v[236:239], off
	s_cbranch_vccnz .LBB0_899
	s_andn2_b64 vcc, exec, s[8:9]
	s_cbranch_vccnz .LBB0_898
	s_barrier
	s_branch .LBB0_898
